# final-layer gather: the 13 next-group u-row loads issued right after the ids are in SGPRs (inside the butterfly) instead of at the step's tail; first-dot waits counted for them only
# speedup vs baseline: 1.0108x; 1.0059x over previous
.LBB0_763:
	s_cmpk_eq_i32 s58, 0x80
	s_cselect_b64 s[12:13], -1, 0
	ds_bpermute_b32 v84, v93, v92
	s_and_b64 vcc, s[12:13], s[48:49]
	v_cndmask_b32_e32 v104, v0, v94, vcc
	v_ashrrev_i32_e32 v105, 31, v104
	s_and_b32 s12, s58, 0x70
	v_lshlrev_b64 v[104:105], 9, v[104:105]
	v_lshl_add_u64 v[104:105], s[94:95], 0, v[104:105]
	s_lshl_b32 s36, s12, 2
	s_waitcnt lgkmcnt(0)
	v_ashrrev_i32_e32 v85, 31, v84
	v_lshl_add_u64 v[104:105], v[104:105], 0, s[36:37]
	v_lshl_add_u64 v[84:85], v[84:85], 3, s[8:9]
	v_lshl_add_u64 v[104:105], v[104:105], 0, v[144:145]
	global_load_dwordx2 v[84:85], v[84:85], off
	s_nop 0
	global_load_dword v86, v[72:73], off
	global_load_dword v92, v[104:105], off
	s_waitcnt vmcnt(19)
	v_dot8_i32_i4 v87, v8, v1, 0
	v_dot8_i32_i4 v104, v8, v88, 0
	v_dot8_i32_i4 v87, v9, v89, v87
	v_dot8_i32_i4 v104, v9, v90, v104
	s_waitcnt vmcnt(19)
	v_dot8_i32_i4 v9, v10, v88, 0
	v_dot8_i32_i4 v9, v11, v90, v9
	v_lshl_add_u32 v87, v87, 4, v104
	v_dot8_i32_i4 v8, v10, v1, 0
	v_dot8_i32_i4 v8, v11, v89, v8
	s_add_i32 s58, s58, 16
	v_lshl_add_u64 v[72:73], v[72:73], 0, 64
	s_waitcnt vmcnt(2)
	v_mul_f32_e32 v85, v91, v85
	v_lshl_add_u32 v104, v8, 4, v9
	v_dot8_i32_i4 v8, v12, v1, 0
	v_dot8_i32_i4 v9, v12, v88, 0
	v_dot8_i32_i4 v8, v13, v89, v8
	v_dot8_i32_i4 v9, v13, v90, v9
	s_waitcnt vmcnt(0)
	v_readlane_b32 s12, v92, 0
	v_readlane_b32 s28, v92, 8
	v_readlane_b32 s30, v92, 9
	v_lshl_add_u32 v105, v8, 4, v9
	v_dot8_i32_i4 v8, v14, v1, 0
	v_dot8_i32_i4 v9, v14, v88, 0
	v_dot8_i32_i4 v8, v15, v89, v8
	v_dot8_i32_i4 v9, v15, v90, v9
	s_ashr_i32 s13, s12, 31
	v_readlane_b32 s14, v92, 1
	s_ashr_i32 s29, s28, 31
	v_lshl_add_u32 v106, v8, 4, v9
	v_dot8_i32_i4 v8, v16, v1, 0
	v_dot8_i32_i4 v9, v16, v88, 0
	v_dot8_i32_i4 v8, v17, v89, v8
	v_dot8_i32_i4 v9, v17, v90, v9
	s_ashr_i32 s31, s30, 31
	v_readlane_b32 s34, v92, 10
	s_lshl_b64 s[12:13], s[12:13], 9
	v_lshl_add_u32 v107, v8, 4, v9
	v_dot8_i32_i4 v8, v18, v1, 0
	v_dot8_i32_i4 v9, v18, v88, 0
	v_dot8_i32_i4 v8, v19, v89, v8
	v_dot8_i32_i4 v9, v19, v90, v9
	s_ashr_i32 s15, s14, 31
	v_readlane_b32 s16, v92, 2
	s_lshl_b64 s[28:29], s[28:29], 9
	v_lshl_add_u32 v108, v8, 4, v9
	v_dot8_i32_i4 v8, v20, v1, 0
	v_dot8_i32_i4 v9, v20, v88, 0
	v_dot8_i32_i4 v8, v21, v89, v8
	v_dot8_i32_i4 v9, v21, v90, v9
	s_lshl_b64 s[30:31], s[30:31], 9
	s_ashr_i32 s35, s34, 31
	v_readlane_b32 s38, v92, 11
	v_lshl_add_u32 v109, v8, 4, v9
	v_dot8_i32_i4 v8, v22, v1, 0
	v_dot8_i32_i4 v9, v22, v88, 0
	v_dot8_i32_i4 v8, v23, v89, v8
	v_dot8_i32_i4 v9, v23, v90, v9
	s_lshl_b64 s[14:15], s[14:15], 9
	s_ashr_i32 s17, s16, 31
	v_readlane_b32 s18, v92, 3
	v_lshl_add_u32 v110, v8, 4, v9
	v_dot8_i32_i4 v8, v24, v1, 0
	v_dot8_i32_i4 v9, v24, v88, 0
	v_dot8_i32_i4 v8, v25, v89, v8
	v_dot8_i32_i4 v9, v25, v90, v9
	s_lshl_b64 s[34:35], s[34:35], 9
	s_ashr_i32 s39, s38, 31
	s_nop 0
	v_lshl_add_u32 v111, v8, 4, v9
	v_dot8_i32_i4 v8, v38, v1, 0
	v_dot8_i32_i4 v9, v38, v88, 0
	v_dot8_i32_i4 v8, v39, v89, v8
	v_dot8_i32_i4 v9, v39, v90, v9
	s_setprio 2
	v_permlane32_swap_b32 v87, v111
	s_nop 1
	v_lshl_add_u32 v112, v8, 4, v9
	v_dot8_i32_i4 v8, v50, v1, 0
	v_dot8_i32_i4 v9, v50, v88, 0
	v_dot8_i32_i4 v8, v51, v89, v8
	v_dot8_i32_i4 v9, v51, v90, v9
	s_waitcnt lgkmcnt(0)
	v_add_u32_e32 v87, v87, v111
	v_permlane32_swap_b32 v104, v112
	v_lshl_add_u32 v113, v8, 4, v9
	v_dot8_i32_i4 v8, v48, v1, 0
	v_dot8_i32_i4 v9, v48, v88, 0
	v_dot8_i32_i4 v8, v49, v89, v8
	v_dot8_i32_i4 v9, v49, v90, v9
	s_waitcnt lgkmcnt(0)
	v_add_u32_e32 v104, v104, v112
	v_permlane32_swap_b32 v105, v113
	v_lshl_add_u32 v114, v8, 4, v9
	v_dot8_i32_i4 v8, v46, v1, 0
	v_dot8_i32_i4 v9, v46, v88, 0
	v_dot8_i32_i4 v8, v47, v89, v8
	v_dot8_i32_i4 v9, v47, v90, v9
	s_waitcnt lgkmcnt(0)
	v_add_u32_e32 v105, v105, v113
	v_permlane32_swap_b32 v106, v114
	v_lshl_add_u32 v115, v8, 4, v9
	v_dot8_i32_i4 v8, v44, v1, 0
	v_dot8_i32_i4 v9, v44, v88, 0
	v_dot8_i32_i4 v8, v45, v89, v8
	v_dot8_i32_i4 v9, v45, v90, v9
	s_waitcnt lgkmcnt(0)
	v_add_u32_e32 v106, v106, v114
	v_permlane32_swap_b32 v107, v115
	v_lshl_add_u32 v116, v8, 4, v9
	v_dot8_i32_i4 v8, v42, v1, 0
	v_dot8_i32_i4 v9, v42, v88, 0
	v_dot8_i32_i4 v8, v43, v89, v8
	v_dot8_i32_i4 v9, v43, v90, v9
	s_waitcnt lgkmcnt(0)
	v_add_u32_e32 v107, v107, v115
	v_permlane32_swap_b32 v108, v116
	v_lshl_add_u32 v117, v8, 4, v9
	v_dot8_i32_i4 v8, v40, v1, 0
	v_dot8_i32_i4 v9, v40, v88, 0
	v_dot8_i32_i4 v8, v41, v89, v8
	v_dot8_i32_i4 v9, v41, v90, v9
	s_waitcnt lgkmcnt(0)
	v_add_u32_e32 v108, v108, v116
	v_permlane32_swap_b32 v109, v117
	v_lshl_add_u32 v118, v8, 4, v9
	s_waitcnt lgkmcnt(0)
	v_add_u32_e32 v109, v109, v117
	v_permlane32_swap_b32 v110, v118
	v_readlane_b32 s50, v92, 12
	s_lshl_b64 s[16:17], s[16:17], 9
	s_ashr_i32 s19, s18, 31
	s_waitcnt lgkmcnt(0)
	v_add_u32_e32 v110, v110, v118
	v_permlane16_swap_b32 v87, v107
	v_readlane_b32 s20, v92, 4
	s_add_u32 s66, s28, s62
	s_addc_u32 s67, s29, s63
	global_load_dwordx2 v[24:25], v121, s[66:67]
	s_add_u32 s66, s30, s62
	s_addc_u32 s67, s31, s63
	global_load_dwordx2 v[38:39], v121, s[66:67]
	s_waitcnt lgkmcnt(0)
	v_add_u32_e32 v87, v87, v107
	v_permlane16_swap_b32 v104, v108
	s_lshl_b64 s[38:39], s[38:39], 9
	s_ashr_i32 s51, s50, 31
	v_readlane_b32 s52, v92, 13
	s_waitcnt lgkmcnt(0)
	v_add_u32_e32 v104, v104, v108
	v_permlane16_swap_b32 v105, v109
	s_lshl_b64 s[18:19], s[18:19], 9
	s_ashr_i32 s21, s20, 31
	v_readlane_b32 s22, v92, 5
	s_waitcnt lgkmcnt(0)
	v_add_u32_e32 v105, v105, v109
	v_permlane16_swap_b32 v106, v110
	s_add_u32 s66, s34, s62
	s_addc_u32 s67, s35, s63
	global_load_dwordx2 v[50:51], v121, s[66:67]
	s_lshl_b64 s[50:51], s[50:51], 9
	s_ashr_i32 s53, s52, 31
	s_waitcnt lgkmcnt(0)
	v_add_u32_e32 v106, v106, v110
	v_cndmask_b32_e64 v107, v87, v105, s[44:45]
	v_cndmask_b32_e64 v87, v105, v87, s[44:45]
	s_nop 0
	v_readlane_b32 s54, v92, 14
	s_lshl_b64 s[20:21], s[20:21], 9
	s_ashr_i32 s23, s22, 31
	v_readlane_b32 s24, v92, 6
	s_waitcnt lgkmcnt(0)
	v_add_u32_dpp v87, v107, v87 row_ror:8 row_mask:0xf bank_mask:0xf
	v_cndmask_b32_e64 v105, v104, v106, s[44:45]
	s_nop 1
	v_cndmask_b32_e64 v104, v106, v104, s[44:45]
	s_lshl_b64 s[52:53], s[52:53], 9
	s_ashr_i32 s55, s54, 31
	v_readlane_b32 s56, v92, 15
	s_waitcnt lgkmcnt(0)
	v_add_u32_dpp v104, v105, v104 row_ror:8 row_mask:0xf bank_mask:0xf
	v_cndmask_b32_e64 v105, v87, v104, s[46:47]
	v_cndmask_b32_e64 v87, v104, v87, s[46:47]
	s_nop 0
	v_mov_b32_dpp v104, v105 row_half_mirror row_mask:0xf bank_mask:0xf
	s_nop 1
	s_lshl_b64 s[22:23], s[22:23], 9
	s_ashr_i32 s25, s24, 31
	v_readlane_b32 s26, v92, 7
	s_lshl_b64 s[54:55], s[54:55], 9
	s_waitcnt lgkmcnt(0)
	v_add_u32_dpp v87, v104, v87 quad_perm:[3,2,1,0] row_mask:0xf bank_mask:0xf
	s_nop 1
	s_ashr_i32 s57, s56, 31
	s_lshl_b64 s[24:25], s[24:25], 9
	s_ashr_i32 s27, s26, 31
	s_lshl_b64 s[56:57], s[56:57], 9
	s_waitcnt lgkmcnt(0)
	v_add_u32_dpp v87, v87, v87 quad_perm:[2,3,0,1] row_mask:0xf bank_mask:0xf
	s_nop 1
	s_lshl_b64 s[26:27], s[26:27], 9
	s_add_u32 s66, s38, s62
	s_addc_u32 s67, s39, s63
	global_load_dwordx2 v[48:49], v121, s[66:67]
	s_add_u32 s66, s50, s62
	s_addc_u32 s67, s51, s63
	global_load_dwordx2 v[46:47], v121, s[66:67]
	s_add_u32 s66, s52, s62
	s_addc_u32 s67, s53, s63
	global_load_dwordx2 v[44:45], v121, s[66:67]
	s_add_u32 s66, s54, s62
	s_addc_u32 s67, s55, s63
	global_load_dwordx2 v[42:43], v121, s[66:67]
	s_add_u32 s66, s56, s62
	s_addc_u32 s67, s57, s63
	global_load_dwordx2 v[40:41], v121, s[66:67]
	s_add_u32 s66, s12, s62
	s_addc_u32 s67, s13, s63
	global_load_dwordx2 v[8:9], v121, s[66:67]
	s_add_u32 s66, s14, s62
	s_addc_u32 s67, s15, s63
	global_load_dwordx2 v[10:11], v121, s[66:67]
	s_add_u32 s66, s16, s62
	s_addc_u32 s67, s17, s63
	global_load_dwordx2 v[12:13], v121, s[66:67]
	s_add_u32 s66, s18, s62
	s_addc_u32 s67, s19, s63
	global_load_dwordx2 v[14:15], v121, s[66:67]
	s_add_u32 s66, s20, s62
	s_addc_u32 s67, s21, s63
	global_load_dwordx2 v[16:17], v121, s[66:67]
	s_add_u32 s66, s22, s62
	s_addc_u32 s67, s23, s63
	global_load_dwordx2 v[18:19], v121, s[66:67]
	s_add_u32 s66, s24, s62
	s_addc_u32 s67, s25, s63
	global_load_dwordx2 v[20:21], v121, s[66:67]
	s_add_u32 s66, s26, s62
	s_addc_u32 s67, s27, s63
	global_load_dwordx2 v[22:23], v121, s[66:67]
	s_waitcnt lgkmcnt(0)
	v_add_u32_dpp v87, v87, v87 quad_perm:[1,0,3,2] row_mask:0xf bank_mask:0xf
	v_cvt_f32_i32_e32 v87, v87
	v_add_f32_e32 v87, v95, v87
	v_mul_f32_e32 v85, v85, v87
	v_mul_f32_e32 v87, 0x3d372713, v85
	v_mul_f32_e32 v87, v85, v87
	v_fma_f32 v87, v85, v87, v85
	v_mul_f32_e32 v87, 0x3fcc422a, v87
	v_mul_f32_e32 v87, 0xbfb8aa3b, v87
	v_exp_f32_e32 v87, v87
	s_nop 0
	v_add_f32_e32 v87, 1.0, v87
	v_rcp_f32_e32 v87, v87
	s_nop 0
	v_pk_mul_f32 v[84:85], v[84:85], v[86:87]
	v_alignbit_b32 v224, v82, v82, 4
	v_pk_mul_f32 v[84:85], v[84:85], v[84:85] op_sel:[0,1] op_sel_hi:[1,0]
	v_cvt_f16_f32_e32 v120, v84
	s_setprio 0
	v_and_b32_e32 v86, 0x7070707, v82
	v_readlane_b32 s36, v120, 0
	v_and_b32_e32 v87, 0x7070707, v224
	v_perm_b32 v86, s2, v205, v86
	v_perm_b32 v87, s2, v205, v87
	v_and_or_b32 v86, v82, s4, v86
	v_and_or_b32 v82, v224, s4, v87
	v_perm_b32 v87, v82, v86, s5
	v_perm_b32 v104, v82, v86, s33
	v_perm_b32 v105, v82, v86, s0
	v_perm_b32 v82, v82, v86, s1
	v_pk_fma_f16 v86, v87, s36, v103 op_sel_hi:[1,0,1]
	v_pk_fma_f16 v87, v104, s36, v102 op_sel_hi:[1,0,1]
	v_alignbit_b32 v225, v83, v83, 4
	v_pk_fma_f16 v82, v82, s36, v100 op_sel_hi:[1,0,1]
	v_and_b32_e32 v100, 0x7070707, v83
	v_and_b32_e32 v102, 0x7070707, v225
	v_perm_b32 v100, s2, v205, v100
	v_perm_b32 v102, s2, v205, v102
	v_and_or_b32 v100, v83, s4, v100
	v_and_or_b32 v83, v225, s4, v102
	v_perm_b32 v102, v83, v100, s5
	v_perm_b32 v103, v83, v100, s33
	v_perm_b32 v104, v83, v100, s0
	v_perm_b32 v83, v83, v100, s1
	v_readlane_b32 s59, v120, 4
	v_alignbit_b32 v224, v80, v80, 4
	v_pk_fma_f16 v101, v105, s36, v101 op_sel_hi:[1,0,1]
	v_pk_fma_f16 v99, v102, s36, v99 op_sel_hi:[1,0,1]
	v_pk_fma_f16 v98, v103, s36, v98 op_sel_hi:[1,0,1]
	v_pk_fma_f16 v97, v104, s36, v97 op_sel_hi:[1,0,1]
	v_pk_fma_f16 v83, v83, s36, v96 op_sel_hi:[1,0,1]
	v_and_b32_e32 v96, 0x7070707, v80
	v_and_b32_e32 v100, 0x7070707, v224
	v_perm_b32 v96, s2, v205, v96
	v_perm_b32 v100, s2, v205, v100
	v_and_or_b32 v96, v80, s4, v96
	v_and_or_b32 v80, v224, s4, v100
	v_perm_b32 v100, v80, v96, s5
	v_perm_b32 v102, v80, v96, s33
	v_perm_b32 v103, v80, v96, s0
	v_perm_b32 v80, v80, v96, s1
	v_pk_fma_f16 v86, v100, s59, v86 op_sel_hi:[1,0,1]
	v_alignbit_b32 v225, v81, v81, 4
	v_pk_fma_f16 v80, v80, s59, v82 op_sel_hi:[1,0,1]
	v_and_b32_e32 v82, 0x7070707, v81
	v_and_b32_e32 v100, 0x7070707, v225
	v_pk_fma_f16 v96, v103, s59, v101 op_sel_hi:[1,0,1]
	v_perm_b32 v82, s2, v205, v82
	v_perm_b32 v100, s2, v205, v100
	v_and_or_b32 v82, v81, s4, v82
	v_and_or_b32 v81, v225, s4, v100
	v_perm_b32 v100, v81, v82, s5
	v_pk_fma_f16 v87, v102, s59, v87 op_sel_hi:[1,0,1]
	v_perm_b32 v101, v81, v82, s33
	v_perm_b32 v102, v81, v82, s0
	v_perm_b32 v81, v81, v82, s1
	v_pk_fma_f16 v82, v100, s59, v99 op_sel_hi:[1,0,1]
	v_readlane_b32 s60, v120, 8
	v_alignbit_b32 v224, v78, v78, 4
	v_pk_fma_f16 v98, v101, s59, v98 op_sel_hi:[1,0,1]
	v_pk_fma_f16 v97, v102, s59, v97 op_sel_hi:[1,0,1]
	v_pk_fma_f16 v81, v81, s59, v83 op_sel_hi:[1,0,1]
	v_and_b32_e32 v85, 0x7070707, v78
	v_and_b32_e32 v99, 0x7070707, v224
	v_perm_b32 v85, s2, v205, v85
	v_perm_b32 v99, s2, v205, v99
	v_and_or_b32 v85, v78, s4, v85
	v_and_or_b32 v78, v224, s4, v99
	v_perm_b32 v99, v78, v85, s5
	v_perm_b32 v100, v78, v85, s33
	v_perm_b32 v101, v78, v85, s0
	v_perm_b32 v78, v78, v85, s1
	v_pk_fma_f16 v85, v99, s60, v86 op_sel_hi:[1,0,1]
	v_pk_fma_f16 v86, v100, s60, v87 op_sel_hi:[1,0,1]
	v_pk_fma_f16 v87, v101, s60, v96 op_sel_hi:[1,0,1]
	v_alignbit_b32 v225, v79, v79, 4
	v_pk_fma_f16 v78, v78, s60, v80 op_sel_hi:[1,0,1]
	v_and_b32_e32 v80, 0x7070707, v79
	v_and_b32_e32 v96, 0x7070707, v225
	v_perm_b32 v80, s2, v205, v80
	v_perm_b32 v96, s2, v205, v96
	v_and_or_b32 v80, v79, s4, v80
	v_and_or_b32 v79, v225, s4, v96
	v_perm_b32 v96, v79, v80, s5
	v_perm_b32 v100, v79, v80, s0
	v_perm_b32 v99, v79, v80, s33
	v_perm_b32 v79, v79, v80, s1
	v_pk_fma_f16 v80, v96, s60, v82 op_sel_hi:[1,0,1]
	v_pk_fma_f16 v96, v100, s60, v97 op_sel_hi:[1,0,1]
	v_readlane_b32 s36, v120, 12
	v_alignbit_b32 v224, v76, v76, 4
	v_pk_fma_f16 v82, v99, s60, v98 op_sel_hi:[1,0,1]
	v_pk_fma_f16 v79, v79, s60, v81 op_sel_hi:[1,0,1]
	v_and_b32_e32 v83, 0x7070707, v76
	v_and_b32_e32 v97, 0x7070707, v224
	v_perm_b32 v83, s2, v205, v83
	v_perm_b32 v97, s2, v205, v97
	v_and_or_b32 v83, v76, s4, v83
	v_and_or_b32 v76, v224, s4, v97
	v_perm_b32 v97, v76, v83, s5
	v_perm_b32 v98, v76, v83, s33
	v_perm_b32 v99, v76, v83, s0
	v_perm_b32 v76, v76, v83, s1
	v_pk_fma_f16 v83, v97, s36, v85 op_sel_hi:[1,0,1]
	v_pk_fma_f16 v85, v98, s36, v86 op_sel_hi:[1,0,1]
	v_pk_fma_f16 v86, v99, s36, v87 op_sel_hi:[1,0,1]
	v_alignbit_b32 v225, v77, v77, 4
	v_pk_fma_f16 v76, v76, s36, v78 op_sel_hi:[1,0,1]
	v_and_b32_e32 v78, 0x7070707, v77
	v_and_b32_e32 v87, 0x7070707, v225
	v_perm_b32 v78, s2, v205, v78
	v_perm_b32 v87, s2, v205, v87
	v_and_or_b32 v78, v77, s4, v78
	v_and_or_b32 v77, v225, s4, v87
	v_perm_b32 v87, v77, v78, s5
	v_perm_b32 v97, v77, v78, s33
	v_perm_b32 v98, v77, v78, s0
	v_perm_b32 v77, v77, v78, s1
	v_pk_fma_f16 v78, v87, s36, v80 op_sel_hi:[1,0,1]
	v_readlane_b32 s59, v120, 16
	v_alignbit_b32 v224, v74, v74, 4
	v_pk_fma_f16 v80, v97, s36, v82 op_sel_hi:[1,0,1]
	v_pk_fma_f16 v82, v98, s36, v96 op_sel_hi:[1,0,1]
	v_pk_fma_f16 v77, v77, s36, v79 op_sel_hi:[1,0,1]
	v_and_b32_e32 v81, 0x7070707, v74
	v_and_b32_e32 v87, 0x7070707, v224
	v_perm_b32 v81, s2, v205, v81
	v_perm_b32 v87, s2, v205, v87
	v_and_or_b32 v81, v74, s4, v81
	v_and_or_b32 v74, v224, s4, v87
	v_perm_b32 v87, v74, v81, s5
	v_perm_b32 v96, v74, v81, s33
	v_perm_b32 v97, v74, v81, s0
	v_perm_b32 v74, v74, v81, s1
	v_pk_fma_f16 v81, v87, s59, v83 op_sel_hi:[1,0,1]
	v_pk_fma_f16 v83, v96, s59, v85 op_sel_hi:[1,0,1]
	v_pk_fma_f16 v85, v97, s59, v86 op_sel_hi:[1,0,1]
	v_alignbit_b32 v225, v75, v75, 4
	v_pk_fma_f16 v74, v74, s59, v76 op_sel_hi:[1,0,1]
	v_and_b32_e32 v76, 0x7070707, v75
	v_and_b32_e32 v86, 0x7070707, v225
	v_perm_b32 v76, s2, v205, v76
	v_perm_b32 v86, s2, v205, v86
	v_and_or_b32 v76, v75, s4, v76
	v_and_or_b32 v75, v225, s4, v86
	v_perm_b32 v86, v75, v76, s5
	v_perm_b32 v87, v75, v76, s33
	v_perm_b32 v96, v75, v76, s0
	v_perm_b32 v75, v75, v76, s1
	v_pk_fma_f16 v76, v86, s59, v78 op_sel_hi:[1,0,1]
	v_pk_fma_f16 v78, v87, s59, v80 op_sel_hi:[1,0,1]
	v_pk_fma_f16 v80, v96, s59, v82 op_sel_hi:[1,0,1]
	v_readlane_b32 s60, v120, 20
	v_alignbit_b32 v224, v70, v70, 4
	v_pk_fma_f16 v75, v75, s59, v77 op_sel_hi:[1,0,1]
	v_and_b32_e32 v79, 0x7070707, v70
	v_and_b32_e32 v82, 0x7070707, v224
	v_perm_b32 v79, s2, v205, v79
	v_perm_b32 v82, s2, v205, v82
	v_and_or_b32 v79, v70, s4, v79
	v_and_or_b32 v70, v224, s4, v82
	v_perm_b32 v82, v70, v79, s5
	v_perm_b32 v86, v70, v79, s33
	v_perm_b32 v87, v70, v79, s0
	v_perm_b32 v70, v70, v79, s1
	v_pk_fma_f16 v79, v82, s60, v81 op_sel_hi:[1,0,1]
	v_pk_fma_f16 v81, v86, s60, v83 op_sel_hi:[1,0,1]
	v_alignbit_b32 v225, v71, v71, 4
	v_pk_fma_f16 v70, v70, s60, v74 op_sel_hi:[1,0,1]
	v_and_b32_e32 v74, 0x7070707, v71
	v_and_b32_e32 v83, 0x7070707, v225
	v_pk_fma_f16 v82, v87, s60, v85 op_sel_hi:[1,0,1]
	v_perm_b32 v74, s2, v205, v74
	v_perm_b32 v83, s2, v205, v83
	v_and_or_b32 v74, v71, s4, v74
	v_and_or_b32 v71, v225, s4, v83
	v_perm_b32 v83, v71, v74, s5
	v_perm_b32 v85, v71, v74, s33
	v_perm_b32 v86, v71, v74, s0
	v_perm_b32 v71, v71, v74, s1
	v_pk_fma_f16 v74, v83, s60, v76 op_sel_hi:[1,0,1]
	v_pk_fma_f16 v76, v85, s60, v78 op_sel_hi:[1,0,1]
	v_pk_fma_f16 v78, v86, s60, v80 op_sel_hi:[1,0,1]
	v_readlane_b32 s36, v120, 24
	v_alignbit_b32 v224, v68, v68, 4
	v_pk_fma_f16 v71, v71, s60, v75 op_sel_hi:[1,0,1]
	v_and_b32_e32 v77, 0x7070707, v68
	v_and_b32_e32 v80, 0x7070707, v224
	v_perm_b32 v77, s2, v205, v77
	v_perm_b32 v80, s2, v205, v80
	v_and_or_b32 v77, v68, s4, v77
	v_and_or_b32 v68, v224, s4, v80
	v_perm_b32 v80, v68, v77, s5
	v_perm_b32 v83, v68, v77, s33
	v_perm_b32 v85, v68, v77, s0
	v_perm_b32 v68, v68, v77, s1
	v_pk_fma_f16 v77, v80, s36, v79 op_sel_hi:[1,0,1]
	v_pk_fma_f16 v79, v83, s36, v81 op_sel_hi:[1,0,1]
	v_alignbit_b32 v225, v69, v69, 4
	v_pk_fma_f16 v68, v68, s36, v70 op_sel_hi:[1,0,1]
	v_and_b32_e32 v70, 0x7070707, v69
	v_and_b32_e32 v81, 0x7070707, v225
	v_pk_fma_f16 v80, v85, s36, v82 op_sel_hi:[1,0,1]
	v_perm_b32 v70, s2, v205, v70
	v_perm_b32 v81, s2, v205, v81
	v_and_or_b32 v70, v69, s4, v70
	v_and_or_b32 v69, v225, s4, v81
	v_perm_b32 v81, v69, v70, s5
	v_perm_b32 v82, v69, v70, s33
	v_perm_b32 v83, v69, v70, s0
	v_perm_b32 v69, v69, v70, s1
	v_pk_fma_f16 v70, v81, s36, v74 op_sel_hi:[1,0,1]
	v_pk_fma_f16 v74, v82, s36, v76 op_sel_hi:[1,0,1]
	v_pk_fma_f16 v76, v83, s36, v78 op_sel_hi:[1,0,1]
	v_readlane_b32 s59, v120, 28
	v_alignbit_b32 v224, v64, v64, 4
	v_pk_fma_f16 v69, v69, s36, v71 op_sel_hi:[1,0,1]
	v_and_b32_e32 v75, 0x7070707, v64
	v_and_b32_e32 v78, 0x7070707, v224
	v_perm_b32 v75, s2, v205, v75
	v_perm_b32 v78, s2, v205, v78
	v_and_or_b32 v75, v64, s4, v75
	v_and_or_b32 v64, v224, s4, v78
	v_perm_b32 v78, v64, v75, s5
	v_perm_b32 v81, v64, v75, s33
	v_perm_b32 v82, v64, v75, s0
	v_perm_b32 v64, v64, v75, s1
	v_pk_fma_f16 v75, v78, s59, v77 op_sel_hi:[1,0,1]
	v_pk_fma_f16 v77, v81, s59, v79 op_sel_hi:[1,0,1]
	v_alignbit_b32 v225, v65, v65, 4
	v_pk_fma_f16 v64, v64, s59, v68 op_sel_hi:[1,0,1]
	v_and_b32_e32 v68, 0x7070707, v65
	v_and_b32_e32 v79, 0x7070707, v225
	v_pk_fma_f16 v78, v82, s59, v80 op_sel_hi:[1,0,1]
	v_perm_b32 v68, s2, v205, v68
	v_perm_b32 v79, s2, v205, v79
	v_and_or_b32 v68, v65, s4, v68
	v_and_or_b32 v65, v225, s4, v79
	v_perm_b32 v79, v65, v68, s5
	v_perm_b32 v80, v65, v68, s33
	v_perm_b32 v81, v65, v68, s0
	v_perm_b32 v65, v65, v68, s1
	v_pk_fma_f16 v68, v79, s59, v70 op_sel_hi:[1,0,1]
	v_pk_fma_f16 v70, v80, s59, v74 op_sel_hi:[1,0,1]
	v_pk_fma_f16 v74, v81, s59, v76 op_sel_hi:[1,0,1]
	v_readlane_b32 s60, v120, 32
	v_alignbit_b32 v224, v62, v62, 4
	v_pk_fma_f16 v65, v65, s59, v69 op_sel_hi:[1,0,1]
	v_and_b32_e32 v71, 0x7070707, v62
	v_and_b32_e32 v76, 0x7070707, v224
	v_perm_b32 v71, s2, v205, v71
	v_perm_b32 v76, s2, v205, v76
	v_and_or_b32 v71, v62, s4, v71
	v_and_or_b32 v62, v224, s4, v76
	v_perm_b32 v76, v62, v71, s5
	v_perm_b32 v79, v62, v71, s33
	v_perm_b32 v80, v62, v71, s0
	v_perm_b32 v62, v62, v71, s1
	v_pk_fma_f16 v71, v76, s60, v75 op_sel_hi:[1,0,1]
	v_pk_fma_f16 v75, v79, s60, v77 op_sel_hi:[1,0,1]
	v_alignbit_b32 v225, v63, v63, 4
	v_pk_fma_f16 v62, v62, s60, v64 op_sel_hi:[1,0,1]
	v_and_b32_e32 v64, 0x7070707, v63
	v_and_b32_e32 v77, 0x7070707, v225
	v_pk_fma_f16 v76, v80, s60, v78 op_sel_hi:[1,0,1]
	v_perm_b32 v64, s2, v205, v64
	v_perm_b32 v77, s2, v205, v77
	v_and_or_b32 v64, v63, s4, v64
	v_and_or_b32 v63, v225, s4, v77
	v_perm_b32 v77, v63, v64, s5
	v_perm_b32 v78, v63, v64, s33
	v_perm_b32 v79, v63, v64, s0
	v_perm_b32 v63, v63, v64, s1
	v_pk_fma_f16 v64, v77, s60, v68 op_sel_hi:[1,0,1]
	v_pk_fma_f16 v68, v78, s60, v70 op_sel_hi:[1,0,1]
	v_pk_fma_f16 v70, v79, s60, v74 op_sel_hi:[1,0,1]
	v_readlane_b32 s36, v120, 36
	v_alignbit_b32 v224, v66, v66, 4
	v_pk_fma_f16 v63, v63, s60, v65 op_sel_hi:[1,0,1]
	v_and_b32_e32 v69, 0x7070707, v66
	v_and_b32_e32 v74, 0x7070707, v224
	v_perm_b32 v69, s2, v205, v69
	v_perm_b32 v74, s2, v205, v74
	v_and_or_b32 v69, v66, s4, v69
	v_and_or_b32 v66, v224, s4, v74
	v_perm_b32 v74, v66, v69, s5
	v_perm_b32 v77, v66, v69, s33
	v_perm_b32 v78, v66, v69, s0
	v_perm_b32 v66, v66, v69, s1
	v_pk_fma_f16 v69, v74, s36, v71 op_sel_hi:[1,0,1]
	v_pk_fma_f16 v71, v77, s36, v75 op_sel_hi:[1,0,1]
	v_alignbit_b32 v225, v67, v67, 4
	v_pk_fma_f16 v62, v66, s36, v62 op_sel_hi:[1,0,1]
	v_and_b32_e32 v66, 0x7070707, v67
	v_and_b32_e32 v75, 0x7070707, v225
	v_pk_fma_f16 v74, v78, s36, v76 op_sel_hi:[1,0,1]
	v_perm_b32 v66, s2, v205, v66
	v_perm_b32 v75, s2, v205, v75
	v_and_or_b32 v66, v67, s4, v66
	v_and_or_b32 v67, v225, s4, v75
	v_perm_b32 v76, v67, v66, s33
	v_perm_b32 v77, v67, v66, s0
	v_perm_b32 v75, v67, v66, s5
	v_perm_b32 v66, v67, v66, s1
	v_pk_fma_f16 v67, v76, s36, v68 op_sel_hi:[1,0,1]
	v_pk_fma_f16 v68, v77, s36, v70 op_sel_hi:[1,0,1]
	v_readlane_b32 s59, v120, 40
	v_alignbit_b32 v224, v60, v60, 4
	v_pk_fma_f16 v64, v75, s36, v64 op_sel_hi:[1,0,1]
	v_pk_fma_f16 v63, v66, s36, v63 op_sel_hi:[1,0,1]
	v_and_b32_e32 v66, 0x7070707, v60
	v_and_b32_e32 v70, 0x7070707, v224
	v_perm_b32 v66, s2, v205, v66
	v_perm_b32 v70, s2, v205, v70
	v_and_or_b32 v66, v60, s4, v66
	v_and_or_b32 v60, v224, s4, v70
	v_perm_b32 v70, v60, v66, s5
	v_perm_b32 v75, v60, v66, s33
	v_perm_b32 v76, v60, v66, s0
	v_perm_b32 v60, v60, v66, s1
	v_pk_fma_f16 v66, v70, s59, v69 op_sel_hi:[1,0,1]
	v_pk_fma_f16 v69, v75, s59, v71 op_sel_hi:[1,0,1]
	v_alignbit_b32 v225, v61, v61, 4
	v_pk_fma_f16 v60, v60, s59, v62 op_sel_hi:[1,0,1]
	v_and_b32_e32 v62, 0x7070707, v61
	v_and_b32_e32 v71, 0x7070707, v225
	v_pk_fma_f16 v70, v76, s59, v74 op_sel_hi:[1,0,1]
	v_perm_b32 v62, s2, v205, v62
	v_perm_b32 v71, s2, v205, v71
	v_and_or_b32 v62, v61, s4, v62
	v_and_or_b32 v61, v225, s4, v71
	v_perm_b32 v71, v61, v62, s5
	v_perm_b32 v74, v61, v62, s33
	v_perm_b32 v75, v61, v62, s0
	v_perm_b32 v61, v61, v62, s1
	v_pk_fma_f16 v62, v71, s59, v64 op_sel_hi:[1,0,1]
	v_pk_fma_f16 v64, v74, s59, v67 op_sel_hi:[1,0,1]
	v_pk_fma_f16 v67, v75, s59, v68 op_sel_hi:[1,0,1]
	v_readlane_b32 s60, v120, 44
	v_alignbit_b32 v224, v58, v58, 4
	v_pk_fma_f16 v61, v61, s59, v63 op_sel_hi:[1,0,1]
	v_and_b32_e32 v65, 0x7070707, v58
	v_and_b32_e32 v68, 0x7070707, v224
	v_perm_b32 v65, s2, v205, v65
	v_perm_b32 v68, s2, v205, v68
	v_and_or_b32 v65, v58, s4, v65
	v_and_or_b32 v58, v224, s4, v68
	v_perm_b32 v68, v58, v65, s5
	v_perm_b32 v71, v58, v65, s33
	v_perm_b32 v74, v58, v65, s0
	v_perm_b32 v58, v58, v65, s1
	v_pk_fma_f16 v65, v68, s60, v66 op_sel_hi:[1,0,1]
	v_pk_fma_f16 v66, v71, s60, v69 op_sel_hi:[1,0,1]
	v_alignbit_b32 v225, v59, v59, 4
	v_pk_fma_f16 v58, v58, s60, v60 op_sel_hi:[1,0,1]
	v_and_b32_e32 v60, 0x7070707, v59
	v_and_b32_e32 v69, 0x7070707, v225
	v_pk_fma_f16 v68, v74, s60, v70 op_sel_hi:[1,0,1]
	v_perm_b32 v60, s2, v205, v60
	v_perm_b32 v69, s2, v205, v69
	v_and_or_b32 v60, v59, s4, v60
	v_and_or_b32 v59, v225, s4, v69
	v_perm_b32 v69, v59, v60, s5
	v_perm_b32 v70, v59, v60, s33
	v_perm_b32 v71, v59, v60, s0
	v_perm_b32 v59, v59, v60, s1
	v_pk_fma_f16 v60, v69, s60, v62 op_sel_hi:[1,0,1]
	v_pk_fma_f16 v62, v70, s60, v64 op_sel_hi:[1,0,1]
	v_pk_fma_f16 v64, v71, s60, v67 op_sel_hi:[1,0,1]
	v_readlane_b32 s36, v120, 48
	v_alignbit_b32 v224, v56, v56, 4
	v_pk_fma_f16 v59, v59, s60, v61 op_sel_hi:[1,0,1]
	v_and_b32_e32 v63, 0x7070707, v56
	v_and_b32_e32 v67, 0x7070707, v224
	v_perm_b32 v63, s2, v205, v63
	v_perm_b32 v67, s2, v205, v67
	v_and_or_b32 v63, v56, s4, v63
	v_and_or_b32 v56, v224, s4, v67
	v_perm_b32 v67, v56, v63, s5
	v_perm_b32 v69, v56, v63, s33
	v_perm_b32 v70, v56, v63, s0
	v_perm_b32 v56, v56, v63, s1
	v_pk_fma_f16 v63, v67, s36, v65 op_sel_hi:[1,0,1]
	v_alignbit_b32 v225, v57, v57, 4
	v_pk_fma_f16 v56, v56, s36, v58 op_sel_hi:[1,0,1]
	v_and_b32_e32 v58, 0x7070707, v57
	v_and_b32_e32 v67, 0x7070707, v225
	v_pk_fma_f16 v65, v69, s36, v66 op_sel_hi:[1,0,1]
	v_pk_fma_f16 v66, v70, s36, v68 op_sel_hi:[1,0,1]
	v_perm_b32 v58, s2, v205, v58
	v_perm_b32 v67, s2, v205, v67
	v_and_or_b32 v58, v57, s4, v58
	v_and_or_b32 v57, v225, s4, v67
	v_perm_b32 v67, v57, v58, s5
	v_perm_b32 v68, v57, v58, s33
	v_perm_b32 v69, v57, v58, s0
	v_perm_b32 v57, v57, v58, s1
	v_pk_fma_f16 v58, v67, s36, v60 op_sel_hi:[1,0,1]
	v_pk_fma_f16 v60, v68, s36, v62 op_sel_hi:[1,0,1]
	v_pk_fma_f16 v62, v69, s36, v64 op_sel_hi:[1,0,1]
	v_readlane_b32 s59, v120, 52
	v_alignbit_b32 v224, v54, v54, 4
	v_pk_fma_f16 v57, v57, s36, v59 op_sel_hi:[1,0,1]
	v_and_b32_e32 v61, 0x7070707, v54
	v_and_b32_e32 v64, 0x7070707, v224
	v_perm_b32 v61, s2, v205, v61
	v_perm_b32 v64, s2, v205, v64
	v_and_or_b32 v61, v54, s4, v61
	v_and_or_b32 v54, v224, s4, v64
	v_perm_b32 v64, v54, v61, s5
	v_perm_b32 v67, v54, v61, s33
	v_perm_b32 v68, v54, v61, s0
	v_perm_b32 v54, v54, v61, s1
	v_pk_fma_f16 v61, v64, s59, v63 op_sel_hi:[1,0,1]
	v_pk_fma_f16 v63, v67, s59, v65 op_sel_hi:[1,0,1]
	v_alignbit_b32 v225, v55, v55, 4
	v_pk_fma_f16 v54, v54, s59, v56 op_sel_hi:[1,0,1]
	v_and_b32_e32 v56, 0x7070707, v55
	v_and_b32_e32 v65, 0x7070707, v225
	v_pk_fma_f16 v64, v68, s59, v66 op_sel_hi:[1,0,1]
	v_perm_b32 v56, s2, v205, v56
	v_perm_b32 v65, s2, v205, v65
	v_and_or_b32 v56, v55, s4, v56
	v_and_or_b32 v55, v225, s4, v65
	v_perm_b32 v65, v55, v56, s5
	v_perm_b32 v66, v55, v56, s33
	v_perm_b32 v67, v55, v56, s0
	v_perm_b32 v55, v55, v56, s1
	v_pk_fma_f16 v56, v65, s59, v58 op_sel_hi:[1,0,1]
	v_pk_fma_f16 v58, v66, s59, v60 op_sel_hi:[1,0,1]
	v_pk_fma_f16 v60, v67, s59, v62 op_sel_hi:[1,0,1]
	v_readlane_b32 s60, v120, 56
	v_alignbit_b32 v224, v52, v52, 4
	v_pk_fma_f16 v55, v55, s59, v57 op_sel_hi:[1,0,1]
	v_and_b32_e32 v59, 0x7070707, v52
	v_and_b32_e32 v62, 0x7070707, v224
	v_perm_b32 v59, s2, v205, v59
	v_perm_b32 v62, s2, v205, v62
	v_and_or_b32 v59, v52, s4, v59
	v_and_or_b32 v52, v224, s4, v62
	v_perm_b32 v62, v52, v59, s5
	v_perm_b32 v65, v52, v59, s33
	v_perm_b32 v66, v52, v59, s0
	v_perm_b32 v52, v52, v59, s1
	v_pk_fma_f16 v59, v62, s60, v61 op_sel_hi:[1,0,1]
	v_pk_fma_f16 v61, v65, s60, v63 op_sel_hi:[1,0,1]
	v_alignbit_b32 v225, v53, v53, 4
	v_pk_fma_f16 v52, v52, s60, v54 op_sel_hi:[1,0,1]
	v_and_b32_e32 v54, 0x7070707, v53
	v_and_b32_e32 v63, 0x7070707, v225
	v_pk_fma_f16 v62, v66, s60, v64 op_sel_hi:[1,0,1]
	v_perm_b32 v54, s2, v205, v54
	v_perm_b32 v63, s2, v205, v63
	v_and_or_b32 v54, v53, s4, v54
	v_and_or_b32 v53, v225, s4, v63
	v_perm_b32 v63, v53, v54, s5
	v_perm_b32 v64, v53, v54, s33
	v_perm_b32 v65, v53, v54, s0
	v_perm_b32 v53, v53, v54, s1
	v_pk_fma_f16 v54, v63, s60, v56 op_sel_hi:[1,0,1]
	v_pk_fma_f16 v56, v64, s60, v58 op_sel_hi:[1,0,1]
	v_pk_fma_f16 v58, v65, s60, v60 op_sel_hi:[1,0,1]
	v_readlane_b32 s36, v120, 60
	v_alignbit_b32 v224, v36, v36, 4
	v_pk_fma_f16 v53, v53, s60, v55 op_sel_hi:[1,0,1]
	v_and_b32_e32 v57, 0x7070707, v36
	v_and_b32_e32 v60, 0x7070707, v224
	v_perm_b32 v57, s2, v205, v57
	v_perm_b32 v60, s2, v205, v60
	v_and_or_b32 v57, v36, s4, v57
	v_and_or_b32 v36, v224, s4, v60
	v_perm_b32 v60, v36, v57, s5
	v_perm_b32 v63, v36, v57, s33
	v_perm_b32 v64, v36, v57, s0
	v_perm_b32 v36, v36, v57, s1
	v_pk_fma_f16 v100, v36, s36, v52 op_sel_hi:[1,0,1]
	v_alignbit_b32 v225, v37, v37, 4
	v_and_b32_e32 v36, 0x7070707, v37
	v_and_b32_e32 v52, 0x7070707, v225
	v_perm_b32 v36, s2, v205, v36
	v_perm_b32 v52, s2, v205, v52
	v_and_or_b32 v36, v37, s4, v36
	v_and_or_b32 v37, v225, s4, v52
	v_pk_fma_f16 v103, v60, s36, v59 op_sel_hi:[1,0,1]
	v_perm_b32 v52, v37, v36, s5
	v_perm_b32 v57, v37, v36, s33
	v_perm_b32 v59, v37, v36, s0
	v_perm_b32 v36, v37, v36, s1
	v_pk_fma_f16 v96, v36, s36, v53 op_sel_hi:[1,0,1]
	s_add_u32 s66, s12, s64
	s_addc_u32 s67, s13, s65
	global_load_dwordx2 v[82:83], v121, s[66:67]
	s_add_u32 s66, s14, s64
	s_addc_u32 s67, s15, s65
	global_load_dwordx2 v[80:81], v121, s[66:67]
	s_add_u32 s66, s16, s64
	s_addc_u32 s67, s17, s65
	global_load_dwordx2 v[78:79], v121, s[66:67]
	s_add_u32 s66, s18, s64
	s_addc_u32 s67, s19, s65
	global_load_dwordx2 v[76:77], v121, s[66:67]
	s_add_u32 s66, s20, s64
	s_addc_u32 s67, s21, s65
	global_load_dwordx2 v[74:75], v121, s[66:67]
	s_add_u32 s66, s22, s64
	s_addc_u32 s67, s23, s65
	global_load_dwordx2 v[70:71], v121, s[66:67]
	v_pk_fma_f16 v101, v64, s36, v62 op_sel_hi:[1,0,1]
	s_add_u32 s66, s24, s64
	s_addc_u32 s67, s25, s65
	global_load_dwordx2 v[68:69], v121, s[66:67]
	s_add_u32 s66, s26, s64
	s_addc_u32 s67, s27, s65
	global_load_dwordx2 v[64:65], v121, s[66:67]
	v_pk_fma_f16 v102, v63, s36, v61 op_sel_hi:[1,0,1]
	s_add_u32 s66, s28, s64
	s_addc_u32 s67, s29, s65
	global_load_dwordx2 v[62:63], v121, s[66:67]
	s_add_u32 s66, s30, s64
	s_addc_u32 s67, s31, s65
	global_load_dwordx2 v[66:67], v121, s[66:67]
	s_add_u32 s66, s34, s64
	s_addc_u32 s67, s35, s65
	global_load_dwordx2 v[60:61], v121, s[66:67]
	v_pk_fma_f16 v97, v59, s36, v58 op_sel_hi:[1,0,1]
	s_add_u32 s66, s38, s64
	s_addc_u32 s67, s39, s65
	global_load_dwordx2 v[58:59], v121, s[66:67]
	v_pk_fma_f16 v98, v57, s36, v56 op_sel_hi:[1,0,1]
	s_add_u32 s66, s50, s64
	s_addc_u32 s67, s51, s65
	global_load_dwordx2 v[56:57], v121, s[66:67]
	v_pk_fma_f16 v99, v52, s36, v54 op_sel_hi:[1,0,1]
	s_add_u32 s66, s52, s64
	s_addc_u32 s67, s53, s65
	global_load_dwordx2 v[54:55], v121, s[66:67]
	s_add_u32 s66, s54, s64
	s_addc_u32 s67, s55, s65
	global_load_dwordx2 v[52:53], v121, s[66:67]
	s_nop 0
	s_nop 0
	s_nop 0
	s_nop 0
	s_nop 0
	s_nop 0
	s_nop 0
	s_add_u32 s66, s56, s64
	s_addc_u32 s67, s57, s65
	global_load_dwordx2 v[36:37], v121, s[66:67]
	s_cmpk_eq_i32 s58, 0x90
	s_cbranch_scc0 .LBB0_763
	v_lshlrev_b64 v[0:1], 2, v[2:3]
	v_lshl_add_u64 v[2:3], v[28:29], 0, v[0:1]
	v_mov_b32_e32 v104, v208
	v_mov_b32_e32 v105, v209
	v_mov_b32_e32 v106, v210
	v_mov_b32_e32 v107, v211
	v_mov_b32_e32 v108, v212
	v_mov_b32_e32 v109, v213
	v_mov_b32_e32 v110, v214
	v_mov_b32_e32 v111, v215
	v_mov_b32_e32 v86, v216
	v_mov_b32_e32 v87, v217
	v_mov_b32_e32 v88, v218
	v_mov_b32_e32 v89, v219
	v_mov_b32_e32 v112, v220
	v_mov_b32_e32 v113, v221
	v_mov_b32_e32 v114, v222
	v_mov_b32_e32 v115, v223
	v_lshl_add_u64 v[72:73], v[32:33], 0, v[0:1]
	v_cvt_f32_f16_sdwa v1, v103 dst_sel:DWORD dst_unused:UNUSED_PAD src0_sel:WORD_1
	v_cvt_f32_f16_e32 v0, v103
	v_cvt_f32_f16_sdwa v91, v102 dst_sel:DWORD dst_unused:UNUSED_PAD src0_sel:WORD_1
	v_cvt_f32_f16_e32 v90, v102
	v_cvt_f32_f16_sdwa v103, v101 dst_sel:DWORD dst_unused:UNUSED_PAD src0_sel:WORD_1
	v_cvt_f32_f16_e32 v102, v101
	v_cvt_f32_f16_sdwa v101, v100 dst_sel:DWORD dst_unused:UNUSED_PAD src0_sel:WORD_1
	v_cvt_f32_f16_e32 v100, v100
	s_mov_b32 s18, 0x800000
	v_readlane_b32 s12, v255, 5
	v_readlane_b32 s13, v255, 6
	v_pk_add_f32 v[86:87], v[86:87], v[102:103]
	v_pk_add_f32 v[84:85], v[112:113], v[0:1]
	v_mov_b32_e32 v102, v85
	v_mov_b32_e32 v103, v87
	v_pk_add_f32 v[90:91], v[114:115], v[90:91]
	v_pk_add_f32 v[88:89], v[88:89], v[100:101]
	v_mov_b32_e32 v100, v84
	v_mov_b32_e32 v101, v86
	v_pk_mul_f32 v[102:103], v[102:103], v[102:103]
	v_mov_b32_e32 v112, v91
	v_pk_fma_f32 v[100:101], v[100:101], v[100:101], v[102:103]
	v_mov_b32_e32 v102, v90
	v_mov_b32_e32 v103, v88
	v_pk_fma_f32 v[100:101], v[102:103], v[102:103], v[100:101]
	v_cvt_f32_f16_sdwa v103, v99 dst_sel:DWORD dst_unused:UNUSED_PAD src0_sel:WORD_1
	v_cvt_f32_f16_e32 v102, v99
	v_cvt_f32_f16_sdwa v99, v98 dst_sel:DWORD dst_unused:UNUSED_PAD src0_sel:WORD_1
	v_cvt_f32_f16_e32 v98, v98
	v_mov_b32_e32 v113, v89
	v_pk_add_f32 v[102:103], v[108:109], v[102:103]
	v_cvt_f32_f16_sdwa v109, v97 dst_sel:DWORD dst_unused:UNUSED_PAD src0_sel:WORD_1
	v_cvt_f32_f16_e32 v108, v97
	v_cvt_f32_f16_sdwa v97, v96 dst_sel:DWORD dst_unused:UNUSED_PAD src0_sel:WORD_1
	v_cvt_f32_f16_e32 v96, v96
	v_pk_add_f32 v[98:99], v[110:111], v[98:99]
	v_pk_add_f32 v[104:105], v[104:105], v[108:109]
	v_mov_b32_e32 v108, v103
	v_mov_b32_e32 v109, v105
	v_pk_add_f32 v[96:97], v[106:107], v[96:97]
	v_mov_b32_e32 v106, v102
	v_mov_b32_e32 v107, v104
	v_pk_mul_f32 v[108:109], v[108:109], v[108:109]
	v_pk_fma_f32 v[100:101], v[112:113], v[112:113], v[100:101]
	v_pk_fma_f32 v[106:107], v[106:107], v[106:107], v[108:109]
	v_mov_b32_e32 v108, v98
	v_mov_b32_e32 v109, v96
	v_mov_b32_e32 v110, v99
	v_mov_b32_e32 v111, v97
	v_pk_fma_f32 v[106:107], v[108:109], v[108:109], v[106:107]
	v_add_f32_e32 v95, v100, v101
	v_pk_fma_f32 v[106:107], v[110:111], v[110:111], v[106:107]
	v_lshl_add_u64 v[34:35], v[34:35], 0, s[12:13]
	v_add_f32_e32 v95, v95, v106
	v_add_f32_e32 v95, v95, v107
	v_mov_b32_e32 v100, v95
	s_nop 1
	v_permlane32_swap_b32 v100, v95
	s_waitcnt lgkmcnt(0)
	v_add_f32_e32 v95, v95, v100
	v_mov_b32_e32 v100, v95
	s_nop 1
	v_permlane16_swap_b32 v100, v95
	s_waitcnt lgkmcnt(0)
	v_add_f32_e32 v95, v95, v100
	s_nop 1
	v_mov_b32_dpp v100, v95 row_ror:8 row_mask:0xf bank_mask:0xf
	s_waitcnt lgkmcnt(0)
	v_add_f32_e32 v95, v95, v100
	s_nop 1
	v_mov_b32_dpp v100, v95 row_half_mirror row_mask:0xf bank_mask:0xf
	s_nop 1
	v_mov_b32_dpp v100, v100 quad_perm:[3,2,1,0] row_mask:0xf bank_mask:0xf
	s_waitcnt lgkmcnt(0)
	v_add_f32_e32 v95, v95, v100
	s_nop 1
	v_mov_b32_dpp v100, v95 quad_perm:[2,3,0,1] row_mask:0xf bank_mask:0xf
	s_waitcnt lgkmcnt(0)
	v_add_f32_e32 v95, v95, v100
	s_nop 1
	v_mov_b32_dpp v100, v95 quad_perm:[1,0,3,2] row_mask:0xf bank_mask:0xf
	s_waitcnt lgkmcnt(0)
	v_add_f32_e32 v95, v95, v100
	v_fmamk_f32 v95, v95, 0x3a800000, v191
	v_cmp_gt_f32_e32 vcc, s18, v95
	v_mul_f32_e32 v100, 0x4b800000, v95
	s_nop 0
	v_cndmask_b32_e32 v95, v95, v100, vcc
	v_rsq_f32_e32 v95, v95
	s_nop 0
	v_mul_f32_e32 v100, 0x45800000, v95
	v_cndmask_b32_e32 v100, v95, v100, vcc
	v_pk_mul_f32 v[84:85], v[84:85], v[100:101] op_sel_hi:[1,0]
	v_pk_mul_f32 v[0:1], v[124:125], v[84:85]
	v_pk_mul_f32 v[84:85], v[90:91], v[100:101] op_sel_hi:[1,0]
	s_nop 0
	v_pk_mul_f32 v[2:3], v[126:127], v[84:85]
	global_store_dwordx4 v[72:73], v[0:3], off
	s_nop 1
	v_pk_mul_f32 v[84:85], v[86:87], v[100:101] op_sel_hi:[1,0]
	v_pk_mul_f32 v[0:1], v[128:129], v[84:85]
	v_pk_mul_f32 v[84:85], v[88:89], v[100:101] op_sel_hi:[1,0]
	s_nop 0
	v_pk_mul_f32 v[2:3], v[130:131], v[84:85]
	global_store_dwordx4 v[72:73], v[0:3], off offset:16
	s_nop 1
	v_pk_mul_f32 v[84:85], v[102:103], v[100:101] op_sel_hi:[1,0]
	v_pk_mul_f32 v[0:1], v[84:85], v[132:133]
	v_pk_mul_f32 v[84:85], v[98:99], v[100:101] op_sel_hi:[1,0]
	s_nop 0
	v_pk_mul_f32 v[2:3], v[84:85], v[134:135]
	global_store_dwordx4 v[72:73], v[0:3], off offset:32
	s_nop 1
	v_pk_mul_f32 v[84:85], v[104:105], v[100:101] op_sel_hi:[1,0]
	v_pk_mul_f32 v[0:1], v[84:85], v[136:137]
	v_pk_mul_f32 v[84:85], v[96:97], v[100:101] op_sel_hi:[1,0]
	s_nop 0
	v_pk_mul_f32 v[2:3], v[84:85], v[138:139]
	global_store_dwordx4 v[72:73], v[0:3], off offset:48
	s_nop 1
	v_mov_b32_e32 v0, v94
	s_andn2_b64 exec, exec, s[10:11]
	s_cbranch_execnz .LBB0_762
